# P1 norm1 latch (layers 1-3): 8 dwordx2 row stores -> 4 dwordx4 stores via adjacent-lane DPP exchange (tests whether the norm phases are request-rate bound); on top of v9_prohoist
# baseline (speedup 1.0000x reference)
.LBB0_265:
	s_or_b64 exec, exec, s[38:39]
	s_mov_b32 s0, 0x3e0f83e1
	v_mul_hi_i32 v2, v40, s0
	v_lshrrev_b32_e32 v38, 31, v2
	v_ashrrev_i32_e32 v2, 11, v2
	v_add_u32_e32 v2, v2, v38
	v_mul_i32_i24_e32 v38, 0x2100, v2
	v_sub_u32_e32 v38, v40, v38
	s_movk_i32 s0, 0xff
	v_subrev_u32_e32 v2, s22, v2
	v_cmp_lt_i32_e32 vcc, s0, v38
	s_waitcnt vmcnt(0)
	v_lshlrev_b32_e32 v66, 16, v26
	v_and_b32_e32 v67, 0xffff0000, v26
	v_cndmask_b32_e32 v2, 2, v2, vcc
	v_lshlrev_b32_e32 v2, 12, v2
	v_add_u32_e32 v90, v124, v2
	v_lshlrev_b32_e32 v74, 16, v27
	v_and_b32_e32 v75, 0xffff0000, v27
	v_lshlrev_b32_e32 v76, 16, v24
	v_and_b32_e32 v77, 0xffff0000, v24
	v_lshlrev_b32_e32 v80, 16, v25
	v_and_b32_e32 v81, 0xffff0000, v25
	ds_read_b128 v[24:27], v90
	ds_read_b128 v[70:73], v90 offset:1024
	v_lshlrev_b32_e32 v38, 16, v28
	v_and_b32_e32 v39, 0xffff0000, v28
	v_lshlrev_b32_e32 v28, 16, v29
	v_and_b32_e32 v29, 0xffff0000, v29
	s_waitcnt lgkmcnt(1)
	v_pk_fma_f32 v[88:89], v[6:7], v[26:27], v[28:29]
	ds_read_b128 v[26:29], v90 offset:2048
	v_pk_fma_f32 v[24:25], v[4:5], v[24:25], v[38:39]
	ds_read_b128 v[4:7], v90 offset:3072
	v_lshlrev_b32_e32 v86, 16, v22
	v_and_b32_e32 v87, 0xffff0000, v22
	s_waitcnt lgkmcnt(2)
	v_pk_fma_f32 v[66:67], v[8:9], v[70:71], v[66:67]
	v_mul_f32_e32 v2, v25, v25
	s_waitcnt lgkmcnt(0)
	v_pk_fma_f32 v[70:71], v[16:17], v[4:5], v[86:87]
	v_mul_f32_e32 v4, v67, v67
	v_pk_fma_f32 v[38:39], v[10:11], v[72:73], v[74:75]
	v_fmac_f32_e32 v2, v24, v24
	v_fmac_f32_e32 v4, v66, v66
	v_fmac_f32_e32 v2, v88, v88
	v_fmac_f32_e32 v4, v38, v38
	v_pk_fma_f32 v[26:27], v[12:13], v[26:27], v[76:77]
	v_fmac_f32_e32 v2, v89, v89
	v_fmac_f32_e32 v4, v39, v39
	v_add_f32_e32 v2, v2, v4
	v_mul_f32_e32 v4, v27, v27
	v_pk_fma_f32 v[28:29], v[14:15], v[28:29], v[80:81]
	v_fmac_f32_e32 v4, v26, v26
	v_fmac_f32_e32 v4, v28, v28
	v_fmac_f32_e32 v4, v29, v29
	v_lshlrev_b32_e32 v22, 16, v23
	v_and_b32_e32 v23, 0xffff0000, v23
	v_add_f32_e32 v2, v2, v4
	v_mul_f32_e32 v4, v71, v71
	v_pk_fma_f32 v[22:23], v[18:19], v[6:7], v[22:23]
	v_fmac_f32_e32 v4, v70, v70
	v_fmac_f32_e32 v4, v22, v22
	v_fmac_f32_e32 v4, v23, v23
	v_add_f32_e32 v2, v2, v4
	v_ashrrev_i32_e32 v41, 31, v40
	v_lshlrev_b64 v[40:41], 11, v[40:41]
	v_add_f32_dpp v2, v2, v2 quad_perm:[1,0,3,2] row_mask:0xf bank_mask:0xf bound_ctrl:1
	v_lshl_add_u64 v[72:73], v[30:31], 0, v[40:41]
	v_cvt_pk_bf16_f32 v133, v88, v89
	v_add_f32_dpp v2, v2, v2 quad_perm:[2,3,0,1] row_mask:0xf bank_mask:0xf bound_ctrl:1
	v_add_u32_e32 v122, 8, v122
	v_mov_b32_e32 v125, v129
	v_add_f32_dpp v2, v2, v2 row_ror:4 row_mask:0xf bank_mask:0xf bound_ctrl:1
	v_mov_b32_e32 v126, v128
	v_mov_b32_e32 v130, v127
	v_add_f32_dpp v2, v2, v2 row_ror:8 row_mask:0xf bank_mask:0xf bound_ctrl:1
	v_mov_b32_e32 v4, v2
	s_nop 1
	v_permlane16_swap_b32_e32 v2, v4
	v_add_f32_e32 v2, v2, v4
	v_mov_b32_e32 v4, v2
	s_nop 1
	v_permlane32_swap_b32_e32 v2, v4
	v_add_f32_e32 v2, v2, v4
	v_fmamk_f32 v2, v2, 0x3a800000, v180
	v_mul_f32_e32 v4, 0x4b800000, v2
	v_cmp_gt_f32_e32 vcc, s33, v2
	v_mov_b32_e32 v76, v108
	v_mov_b32_e32 v77, v109
	v_cndmask_b32_e32 v2, v2, v4, vcc
	v_rsq_f32_e32 v2, v2
	v_mov_b32_e32 v86, v84
	v_mov_b32_e32 v87, v85
	v_mov_b32_e32 v91, v83
	v_mul_f32_e32 v4, 0x45800000, v2
	v_cndmask_b32_e32 v2, v2, v4, vcc
	v_cvt_pk_bf16_f32 v132, v24, v25
	s_nop 0
	ds_read_b128 v[4:7], v90 offset:12288
	ds_read_b128 v[8:11], v90 offset:24576
	v_pk_mul_f32 v[24:25], v[24:25], v[2:3] op_sel_hi:[1,0]
	v_pk_mul_f32 v[74:75], v[88:89], v[2:3] op_sel_hi:[1,0]
	ds_read_b128 v[12:15], v90 offset:13312
	ds_read_b128 v[16:19], v90 offset:25600
	v_cmp_le_i32_e32 vcc, s23, v122
	s_waitcnt lgkmcnt(2)
	v_pk_fma_f32 v[6:7], v[6:7], v[74:75], v[10:11]
	v_pk_fma_f32 v[4:5], v[4:5], v[24:25], v[8:9]
	v_lshl_add_u64 v[24:25], v[36:37], 0, v[40:41]
	v_cvt_pk_bf16_f32 v140, v4, v5
	v_cvt_pk_bf16_f32 v141, v6, v7
	s_nop 0
	v_cvt_pk_bf16_f32 v134, v66, v67
	v_cvt_pk_bf16_f32 v135, v38, v39
	s_nop 0
	v_pk_mul_f32 v[4:5], v[66:67], v[2:3] op_sel_hi:[1,0]
	v_pk_mul_f32 v[6:7], v[38:39], v[2:3] op_sel_hi:[1,0]
	s_waitcnt lgkmcnt(0)
	v_pk_fma_f32 v[4:5], v[12:13], v[4:5], v[16:17]
	v_pk_fma_f32 v[6:7], v[14:15], v[6:7], v[18:19]
	v_cvt_pk_bf16_f32 v142, v4, v5
	v_cvt_pk_bf16_f32 v143, v6, v7
	s_nop 0
	v_cvt_pk_bf16_f32 v136, v26, v27
	v_cvt_pk_bf16_f32 v137, v28, v29
	s_nop 0
	ds_read_b128 v[4:7], v90 offset:14336
	ds_read_b128 v[8:11], v90 offset:26624
	v_pk_mul_f32 v[26:27], v[26:27], v[2:3] op_sel_hi:[1,0]
	v_pk_mul_f32 v[28:29], v[28:29], v[2:3] op_sel_hi:[1,0]
	ds_read_b128 v[12:15], v90 offset:15360
	ds_read_b128 v[16:19], v90 offset:27648
	s_or_b64 s[34:35], vcc, s[34:35]
	s_waitcnt lgkmcnt(2)
	v_pk_fma_f32 v[6:7], v[6:7], v[28:29], v[10:11]
	v_pk_fma_f32 v[4:5], v[4:5], v[26:27], v[8:9]
	v_mov_b32_e32 v8, v21
	v_cvt_pk_bf16_f32 v144, v4, v5
	v_cvt_pk_bf16_f32 v145, v6, v7
	s_nop 0
	v_cvt_pk_bf16_f32 v138, v70, v71
	v_cvt_pk_bf16_f32 v139, v22, v23
	s_nop 0
	v_pk_mul_f32 v[4:5], v[70:71], v[2:3] op_sel_hi:[1,0]
	v_pk_mul_f32 v[6:7], v[22:23], v[2:3] op_sel_hi:[1,0]
	s_waitcnt lgkmcnt(0)
	v_pk_fma_f32 v[4:5], v[4:5], v[12:13], v[16:17]
	v_pk_fma_f32 v[6:7], v[6:7], v[14:15], v[18:19]
	v_cvt_pk_bf16_f32 v146, v4, v5
	v_cvt_pk_bf16_f32 v147, v6, v7
	s_nop 0
	s_nop 1
	v_mbcnt_lo_u32_b32 v131, -1, 0
	v_mbcnt_hi_u32_b32 v131, -1, v131
	v_and_b32_e32 v131, 1, v131
	v_cmp_ne_u32_e64 s[0:1], 0, v131
	v_mul_u32_u24_e32 v156, 0x1f8, v131
	v_mov_b32_e32 v157, 0
	v_lshl_add_u64 v[148:149], v[72:73], 0, v[156:157]
	v_lshl_add_u64 v[150:151], v[24:25], 0, v[156:157]
	v_mov_b32_dpp v152, v134 quad_perm:[1,0,3,2] row_mask:0xf bank_mask:0xf
	v_mov_b32_dpp v153, v135 quad_perm:[1,0,3,2] row_mask:0xf bank_mask:0xf
	v_mov_b32_dpp v154, v132 quad_perm:[1,0,3,2] row_mask:0xf bank_mask:0xf
	v_mov_b32_dpp v155, v133 quad_perm:[1,0,3,2] row_mask:0xf bank_mask:0xf
	v_cndmask_b32_e64 v152, v132, v152, s[0:1]
	v_cndmask_b32_e64 v153, v133, v153, s[0:1]
	v_cndmask_b32_e64 v154, v154, v134, s[0:1]
	v_cndmask_b32_e64 v155, v155, v135, s[0:1]
	global_store_dwordx4 v[148:149], v[152:155], off
	s_nop 1
	v_mov_b32_dpp v152, v138 quad_perm:[1,0,3,2] row_mask:0xf bank_mask:0xf
	v_mov_b32_dpp v153, v139 quad_perm:[1,0,3,2] row_mask:0xf bank_mask:0xf
	v_mov_b32_dpp v154, v136 quad_perm:[1,0,3,2] row_mask:0xf bank_mask:0xf
	v_mov_b32_dpp v155, v137 quad_perm:[1,0,3,2] row_mask:0xf bank_mask:0xf
	v_cndmask_b32_e64 v152, v136, v152, s[0:1]
	v_cndmask_b32_e64 v153, v137, v153, s[0:1]
	v_cndmask_b32_e64 v154, v154, v138, s[0:1]
	v_cndmask_b32_e64 v155, v155, v139, s[0:1]
	global_store_dwordx4 v[148:149], v[152:155], off offset:1024
	s_nop 1
	v_mov_b32_dpp v152, v142 quad_perm:[1,0,3,2] row_mask:0xf bank_mask:0xf
	v_mov_b32_dpp v153, v143 quad_perm:[1,0,3,2] row_mask:0xf bank_mask:0xf
	v_mov_b32_dpp v154, v140 quad_perm:[1,0,3,2] row_mask:0xf bank_mask:0xf
	v_mov_b32_dpp v155, v141 quad_perm:[1,0,3,2] row_mask:0xf bank_mask:0xf
	v_cndmask_b32_e64 v152, v140, v152, s[0:1]
	v_cndmask_b32_e64 v153, v141, v153, s[0:1]
	v_cndmask_b32_e64 v154, v154, v142, s[0:1]
	v_cndmask_b32_e64 v155, v155, v143, s[0:1]
	global_store_dwordx4 v[150:151], v[152:155], off
	s_nop 1
	v_mov_b32_dpp v152, v146 quad_perm:[1,0,3,2] row_mask:0xf bank_mask:0xf
	v_mov_b32_dpp v153, v147 quad_perm:[1,0,3,2] row_mask:0xf bank_mask:0xf
	v_mov_b32_dpp v154, v144 quad_perm:[1,0,3,2] row_mask:0xf bank_mask:0xf
	v_mov_b32_dpp v155, v145 quad_perm:[1,0,3,2] row_mask:0xf bank_mask:0xf
	v_cndmask_b32_e64 v152, v144, v152, s[0:1]
	v_cndmask_b32_e64 v153, v145, v153, s[0:1]
	v_cndmask_b32_e64 v154, v154, v146, s[0:1]
	v_cndmask_b32_e64 v155, v155, v147, s[0:1]
	global_store_dwordx4 v[150:151], v[152:155], off offset:1024
	s_nop 1
	v_mov_b32_e32 v40, v20
	v_mov_b32_e32 v20, v116
	v_mov_b32_e32 v41, v123
	v_mov_b32_e32 v123, v117
	v_mov_b64_e32 v[38:39], v[114:115]
	v_mov_b32_e32 v70, v112
	v_mov_b32_e32 v71, v113
	v_mov_b32_e32 v72, v110
	v_mov_b32_e32 v73, v111
	v_mov_b32_e32 v74, v106
	v_mov_b32_e32 v75, v107
	v_mov_b32_e32 v66, v68
	v_mov_b32_e32 v67, v69
	v_mov_b32_e32 v90, v82
	v_mov_b32_e32 v92, v78
	v_mov_b32_e32 v93, v79
	v_mov_b32_e32 v80, v64
	v_mov_b32_e32 v81, v65
	v_mov_b32_e32 v88, v62
	v_mov_b32_e32 v89, v63
	v_mov_b32_e32 v96, v60
	v_mov_b32_e32 v97, v61
	v_mov_b32_e32 v100, v58
	v_mov_b32_e32 v101, v59
	v_mov_b32_e32 v94, v56
	v_mov_b32_e32 v95, v57
	v_mov_b32_e32 v98, v54
	v_mov_b32_e32 v99, v55
	v_mov_b32_e32 v102, v52
	v_mov_b32_e32 v103, v53
	v_mov_b32_e32 v104, v50
	v_mov_b32_e32 v105, v51
	v_mov_b32_e32 v28, v42
	v_mov_b32_e32 v29, v43
	v_mov_b32_e32 v26, v44
	v_mov_b32_e32 v27, v45
	v_mov_b32_e32 v24, v46
	v_mov_b32_e32 v25, v47
	v_mov_b32_e32 v22, v48
	v_mov_b32_e32 v23, v49
	s_andn2_b64 exec, exec, s[34:35]
	s_cbranch_execz .LBB0_292
